# GLA phase A first MFMA series (4 groups): 12 LDS operand reads issued up front with counted waits, on top of v73
# speedup vs baseline: 1.0096x; 1.0019x over previous
.LBB0_813:
	s_or_b64 exec, exec, s[84:85]
	s_waitcnt lgkmcnt(0)
	s_barrier
	ds_read_b128 v[136:139], v103 offset:32768
	ds_read_b128 v[140:143], v104 offset:50176
	ds_read_b128 v[144:147], v104 offset:51264
	ds_read_b128 v[148:151], v103 offset:32832
	ds_read_b128 v[152:155], v104 offset:50240
	ds_read_b128 v[156:159], v104 offset:51328
	ds_read_b128 v[160:163], v103 offset:32896
	ds_read_b128 v[164:167], v104 offset:50304
	ds_read_b128 v[168:171], v104 offset:51392
	ds_read_b128 v[172:175], v103 offset:32960
	ds_read_b128 v[176:179], v104 offset:50368
	ds_read_b128 v[180:183], v104 offset:51456
	s_waitcnt lgkmcnt(10)
	v_mfma_f32_16x16x32_bf16 v[4:7], v[140:143], v[136:139], 0
	s_lshl_b32 s76, s89, 5
	s_waitcnt lgkmcnt(9)
	v_mfma_f32_16x16x32_bf16 v[0:3], v[144:147], v[136:139], 0
	s_waitcnt lgkmcnt(7)
	v_mfma_f32_16x16x32_bf16 v[4:7], v[152:155], v[148:151], v[4:7]
	s_waitcnt lgkmcnt(6)
	v_mfma_f32_16x16x32_bf16 v[0:3], v[156:159], v[148:151], v[0:3]
	s_waitcnt lgkmcnt(4)
	v_mfma_f32_16x16x32_bf16 v[4:7], v[164:167], v[160:163], v[4:7]
	s_waitcnt lgkmcnt(3)
	v_mfma_f32_16x16x32_bf16 v[0:3], v[168:171], v[160:163], v[0:3]
	s_waitcnt lgkmcnt(1)
	v_mfma_f32_16x16x32_bf16 v[4:7], v[176:179], v[172:175], v[4:7]
	v_add_u32_e32 v14, 0, v94
	s_waitcnt lgkmcnt(0)
	v_mfma_f32_16x16x32_bf16 v[0:3], v[180:183], v[172:175], v[0:3]
	v_cndmask_b32_e64 v8, 0, 1, s[8:9]
	v_cndmask_b32_e64 v9, 0, 1, s[10:11]
	v_cndmask_b32_e64 v8, v9, v8, s[42:43]
	v_and_b32_e32 v8, 1, v8
	v_cmp_eq_u32_e32 vcc, 1, v8
	v_cndmask_b32_e64 v8, 0, 1, s[12:13]
	v_cndmask_b32_e64 v9, 0, 1, s[14:15]
	v_cndmask_b32_e64 v8, v9, v8, s[42:43]
	v_and_b32_e32 v8, 1, v8
	v_cndmask_b32_e32 v4, 0, v4, vcc
	v_cmp_eq_u32_e32 vcc, 1, v8
	v_cndmask_b32_e64 v8, 0, 1, s[16:17]
	v_cndmask_b32_e64 v9, 0, 1, s[18:19]
	v_cndmask_b32_e64 v8, v9, v8, s[42:43]
	v_and_b32_e32 v8, 1, v8
	v_cndmask_b32_e32 v5, 0, v5, vcc
	v_cmp_eq_u32_e32 vcc, 1, v8
	v_cndmask_b32_e64 v8, 0, 1, s[20:21]
	v_cndmask_b32_e64 v9, 0, 1, s[22:23]
	v_cndmask_b32_e64 v8, v9, v8, s[42:43]
	v_and_b32_e32 v8, 1, v8
	v_cndmask_b32_e32 v6, 0, v6, vcc
	v_cmp_eq_u32_e32 vcc, 1, v8
	v_cndmask_b32_e64 v8, 0, 1, s[24:25]
	v_cndmask_b32_e64 v9, 0, 1, s[26:27]
	v_cndmask_b32_e64 v8, v9, v8, s[42:43]
	v_and_b32_e32 v8, 1, v8
	v_cndmask_b32_e32 v7, 0, v7, vcc
	v_cmp_eq_u32_e32 vcc, 1, v8
	v_cndmask_b32_e64 v9, 0, 1, s[30:31]
	s_nop 0
	v_cndmask_b32_e32 v8, 0, v0, vcc
	v_cndmask_b32_e64 v0, 0, 1, s[28:29]
	v_cndmask_b32_e64 v0, v9, v0, s[42:43]
	v_and_b32_e32 v0, 1, v0
	v_cmp_eq_u32_e32 vcc, 1, v0
	v_cndmask_b32_e64 v0, 0, 1, s[34:35]
	s_nop 0
	v_cndmask_b32_e32 v9, 0, v1, vcc
	v_cndmask_b32_e64 v1, 0, 1, s[36:37]
	v_cndmask_b32_e64 v0, v1, v0, s[42:43]
	v_and_b32_e32 v0, 1, v0
	v_cmp_eq_u32_e32 vcc, 1, v0
	v_cndmask_b32_e64 v0, 0, 1, s[38:39]
	v_cndmask_b32_e64 v1, 0, 1, s[40:41]
	v_cndmask_b32_e64 v0, v1, v0, s[42:43]
	v_and_b32_e32 v0, 1, v0
	v_cndmask_b32_e32 v10, 0, v2, vcc
	v_cmp_eq_u32_e32 vcc, 1, v0
	v_cvt_pk_bf16_f32 v0, v4, v5
	v_cvt_pk_bf16_f32 v1, v6, v7
	v_cndmask_b32_e32 v3, 0, v3, vcc
	v_cvt_pk_bf16_f32 v2, v8, v9
	v_cvt_pk_bf16_f32 v3, v10, v3
	v_add_u32_e32 v4, s88, v94
	ds_write_b128 v4, v[0:3]
	v_add_u32_e32 v0, 0x15000, v14
	s_waitcnt lgkmcnt(0)
	s_barrier
	ds_read_b128 v[0:3], v0
	s_lshl_b64 s[82:83], s[82:83], 11
	v_lshlrev_b32_e32 v8, 5, v56
	v_mov_b32_e32 v9, v97
	v_lshl_add_u64 v[8:9], s[82:83], 0, v[8:9]
	v_add_u32_e32 v4, 0x16000, v14
	v_lshl_add_u64 v[10:11], v[70:71], 0, s[76:77]
	ds_read_b128 v[4:7], v4
	v_lshl_add_u64 v[12:13], v[10:11], 0, v[8:9]
	s_waitcnt lgkmcnt(1)
	v_mfma_f32_16x16x32_bf16 v[8:11], v[44:47], v[0:3], 0
	s_lshl_b64 s[42:43], s[92:93], 16
	s_add_i32 s92, s92, s96
	s_cmpk_lt_i32 s92, 0x480
	v_mfma_f32_16x16x32_bf16 v[0:3], v[36:39], v[0:3], 0
	s_waitcnt lgkmcnt(0)
	v_mfma_f32_16x16x32_bf16 v[0:3], v[32:35], v[4:7], v[0:3]
	v_mfma_f32_16x16x32_bf16 v[8:11], v[40:43], v[4:7], v[8:11]
	v_add_u32_e32 v4, 0x16400, v14
	s_nop 5
	v_cvt_pk_bf16_f32 v0, v0, v1
	v_cvt_pk_bf16_f32 v1, v2, v3
	global_store_dwordx2 v[12:13], v[0:1], off offset:512
	v_add_u32_e32 v0, 0x15400, v14
	ds_read_b128 v[0:3], v0
	ds_read_b128 v[4:7], v4
	v_cvt_pk_bf16_f32 v8, v8, v9
	v_cvt_pk_bf16_f32 v9, v10, v11
	global_store_dwordx2 v[12:13], v[8:9], off
	s_waitcnt lgkmcnt(1)
	v_mfma_f32_16x16x32_bf16 v[8:11], v[44:47], v[0:3], 0
	v_mfma_f32_16x16x32_bf16 v[0:3], v[36:39], v[0:3], 0
	s_waitcnt lgkmcnt(0)
	v_mfma_f32_16x16x32_bf16 v[8:11], v[40:43], v[4:7], v[8:11]
	v_mfma_f32_16x16x32_bf16 v[0:3], v[32:35], v[4:7], v[0:3]
	v_add_u32_e32 v4, 0x16800, v14
	s_nop 5
	v_cvt_pk_bf16_f32 v8, v8, v9
	v_cvt_pk_bf16_f32 v9, v10, v11
	v_add_co_u32_e32 v10, vcc, s65, v12
	ds_read_b128 v[4:7], v4
	s_nop 0
	v_addc_co_u32_e32 v11, vcc, 0, v13, vcc
	v_cvt_pk_bf16_f32 v0, v0, v1
	v_cvt_pk_bf16_f32 v1, v2, v3
	global_store_dwordx2 v[10:11], v[0:1], off offset:512
	v_add_u32_e32 v0, 0x15800, v14
	ds_read_b128 v[0:3], v0
	global_store_dwordx2 v[10:11], v[8:9], off
	s_waitcnt lgkmcnt(0)
	v_mfma_f32_16x16x32_bf16 v[8:11], v[44:47], v[0:3], 0
	v_mfma_f32_16x16x32_bf16 v[0:3], v[36:39], v[0:3], 0
	v_mfma_f32_16x16x32_bf16 v[8:11], v[40:43], v[4:7], v[8:11]
	v_mfma_f32_16x16x32_bf16 v[0:3], v[32:35], v[4:7], v[0:3]
	v_add_u32_e32 v4, 0x16c00, v14
	s_nop 5
	v_cvt_pk_bf16_f32 v8, v8, v9
	v_cvt_pk_bf16_f32 v9, v10, v11
	v_add_co_u32_e32 v10, vcc, s49, v12
	ds_read_b128 v[4:7], v4
	s_nop 0
	v_addc_co_u32_e32 v11, vcc, 0, v13, vcc
	v_cvt_pk_bf16_f32 v0, v0, v1
	v_cvt_pk_bf16_f32 v1, v2, v3
	global_store_dwordx2 v[10:11], v[0:1], off offset:512
	v_add_u32_e32 v0, 0x15c00, v14
	ds_read_b128 v[0:3], v0
	global_store_dwordx2 v[10:11], v[8:9], off
	s_waitcnt lgkmcnt(0)
	v_mfma_f32_16x16x32_bf16 v[8:11], v[44:47], v[0:3], 0
	v_mfma_f32_16x16x32_bf16 v[0:3], v[36:39], v[0:3], 0
	v_mfma_f32_16x16x32_bf16 v[8:11], v[40:43], v[4:7], v[8:11]
	v_mfma_f32_16x16x32_bf16 v[0:3], v[32:35], v[4:7], v[0:3]
	s_nop 6
	v_cvt_pk_bf16_f32 v8, v8, v9
	v_cvt_pk_bf16_f32 v9, v10, v11
	v_add_co_u32_e32 v10, vcc, s64, v12
	v_cvt_pk_bf16_f32 v0, v0, v1
	s_nop 0
	v_addc_co_u32_e32 v11, vcc, 0, v13, vcc
	v_cvt_pk_bf16_f32 v1, v2, v3
	global_store_dwordx2 v[10:11], v[8:9], off
	global_store_dwordx2 v[10:11], v[0:1], off offset:512
	ds_read_b128 v[136:139], v105
	ds_read_b128 v[140:143], v105 offset:64
	ds_read_b128 v[144:147], v105 offset:2304
	ds_read_b128 v[148:151], v105 offset:2368
	ds_read_b128 v[152:155], v105 offset:4608
	ds_read_b128 v[156:159], v105 offset:4672
	ds_read_b128 v[160:163], v105 offset:6912
	ds_read_b128 v[164:167], v105 offset:6976
	ds_read_b128 v[168:171], v105 offset:9216
	ds_read_b128 v[172:175], v105 offset:9280
	ds_read_b128 v[176:179], v105 offset:11520
	ds_read_b128 v[180:183], v105 offset:11584
	ds_read_b128 v[184:187], v105 offset:13824
	ds_read_b128 v[188:191], v105 offset:13888
	ds_read_b128 v[192:195], v105 offset:16128
	ds_read_b128 v[196:199], v105 offset:16192
	s_waitcnt lgkmcnt(15)
	v_mfma_f32_16x16x32_bf16 v[0:3], v[136:139], v[44:47], 0
	s_waitcnt lgkmcnt(15)
	v_mfma_f32_16x16x32_bf16 v[4:7], v[136:139], v[36:39], 0
	s_waitcnt lgkmcnt(14)
	v_mfma_f32_16x16x32_bf16 v[0:3], v[140:143], v[40:43], v[0:3]
	s_waitcnt lgkmcnt(14)
	v_mfma_f32_16x16x32_bf16 v[4:7], v[140:143], v[32:35], v[4:7]
	s_nop 6
	v_cvt_pk_bf16_f32 v12, v0, v1
	v_lshl_add_u64 v[0:1], s[42:43], 0, v[88:89]
	v_cvt_pk_bf16_f32 v13, v2, v3
	v_lshl_add_u64 v[2:3], v[72:73], 0, v[0:1]
	v_or_b32_e32 v0, 0x1000, v0
	v_cvt_pk_bf16_f32 v4, v4, v5
	v_cvt_pk_bf16_f32 v5, v6, v7
	v_lshl_add_u64 v[6:7], v[72:73], 0, v[0:1]
	global_store_dwordx2 v[2:3], v[12:13], off
	global_store_dwordx2 v[6:7], v[4:5], off
	s_waitcnt lgkmcnt(13)
	v_mfma_f32_16x16x32_bf16 v[12:15], v[144:147], v[44:47], 0
	s_waitcnt lgkmcnt(13)
	v_mfma_f32_16x16x32_bf16 v[4:7], v[144:147], v[36:39], 0
	s_waitcnt lgkmcnt(12)
	v_mfma_f32_16x16x32_bf16 v[12:15], v[148:151], v[40:43], v[12:15]
	s_waitcnt lgkmcnt(12)
	v_mfma_f32_16x16x32_bf16 v[4:7], v[148:151], v[32:35], v[4:7]
	s_nop 6
	v_cvt_pk_bf16_f32 v12, v12, v13
	v_cvt_pk_bf16_f32 v13, v14, v15
	v_cvt_pk_bf16_f32 v4, v4, v5
	v_cvt_pk_bf16_f32 v5, v6, v7
	v_lshl_add_u64 v[6:7], v[74:75], 0, v[0:1]
	global_store_dwordx2 v[2:3], v[12:13], off offset:512
	global_store_dwordx2 v[6:7], v[4:5], off
	s_waitcnt lgkmcnt(11)
	v_mfma_f32_16x16x32_bf16 v[12:15], v[152:155], v[44:47], 0
	s_waitcnt lgkmcnt(11)
	v_mfma_f32_16x16x32_bf16 v[4:7], v[152:155], v[36:39], 0
	s_waitcnt lgkmcnt(10)
	v_mfma_f32_16x16x32_bf16 v[12:15], v[156:159], v[40:43], v[12:15]
	s_waitcnt lgkmcnt(10)
	v_mfma_f32_16x16x32_bf16 v[4:7], v[156:159], v[32:35], v[4:7]
	s_nop 6
	v_cvt_pk_bf16_f32 v12, v12, v13
	v_cvt_pk_bf16_f32 v13, v14, v15
	v_cvt_pk_bf16_f32 v4, v4, v5
	v_cvt_pk_bf16_f32 v5, v6, v7
	v_lshl_add_u64 v[6:7], v[76:77], 0, v[0:1]
	global_store_dwordx2 v[2:3], v[12:13], off offset:1024
	global_store_dwordx2 v[6:7], v[4:5], off
	s_waitcnt lgkmcnt(9)
	v_mfma_f32_16x16x32_bf16 v[12:15], v[160:163], v[44:47], 0
	s_waitcnt lgkmcnt(9)
	v_mfma_f32_16x16x32_bf16 v[4:7], v[160:163], v[36:39], 0
	s_waitcnt lgkmcnt(8)
	v_mfma_f32_16x16x32_bf16 v[12:15], v[164:167], v[40:43], v[12:15]
	s_waitcnt lgkmcnt(8)
	v_mfma_f32_16x16x32_bf16 v[4:7], v[164:167], v[32:35], v[4:7]
	s_nop 6
	v_cvt_pk_bf16_f32 v12, v12, v13
	v_cvt_pk_bf16_f32 v13, v14, v15
	v_cvt_pk_bf16_f32 v4, v4, v5
	v_cvt_pk_bf16_f32 v5, v6, v7
	v_lshl_add_u64 v[6:7], v[78:79], 0, v[0:1]
	global_store_dwordx2 v[2:3], v[12:13], off offset:1536
	global_store_dwordx2 v[6:7], v[4:5], off
	s_waitcnt lgkmcnt(7)
	v_mfma_f32_16x16x32_bf16 v[12:15], v[168:171], v[44:47], 0
	s_waitcnt lgkmcnt(7)
	v_mfma_f32_16x16x32_bf16 v[4:7], v[168:171], v[36:39], 0
	s_waitcnt lgkmcnt(6)
	v_mfma_f32_16x16x32_bf16 v[12:15], v[172:175], v[40:43], v[12:15]
	s_waitcnt lgkmcnt(6)
	v_mfma_f32_16x16x32_bf16 v[4:7], v[172:175], v[32:35], v[4:7]
	s_nop 6
	v_cvt_pk_bf16_f32 v12, v12, v13
	v_cvt_pk_bf16_f32 v13, v14, v15
	v_cvt_pk_bf16_f32 v4, v4, v5
	v_cvt_pk_bf16_f32 v5, v6, v7
	v_lshl_add_u64 v[6:7], v[80:81], 0, v[0:1]
	global_store_dwordx2 v[2:3], v[12:13], off offset:2048
	global_store_dwordx2 v[6:7], v[4:5], off
	s_waitcnt lgkmcnt(5)
	v_mfma_f32_16x16x32_bf16 v[12:15], v[176:179], v[44:47], 0
	s_waitcnt lgkmcnt(5)
	v_mfma_f32_16x16x32_bf16 v[4:7], v[176:179], v[36:39], 0
	s_waitcnt lgkmcnt(4)
	v_mfma_f32_16x16x32_bf16 v[12:15], v[180:183], v[40:43], v[12:15]
	s_waitcnt lgkmcnt(4)
	v_mfma_f32_16x16x32_bf16 v[4:7], v[180:183], v[32:35], v[4:7]
	s_nop 6
	v_cvt_pk_bf16_f32 v12, v12, v13
	v_cvt_pk_bf16_f32 v13, v14, v15
	v_cvt_pk_bf16_f32 v4, v4, v5
	v_cvt_pk_bf16_f32 v5, v6, v7
	v_lshl_add_u64 v[6:7], v[82:83], 0, v[0:1]
	global_store_dwordx2 v[2:3], v[12:13], off offset:2560
	global_store_dwordx2 v[6:7], v[4:5], off
	s_waitcnt lgkmcnt(3)
	v_mfma_f32_16x16x32_bf16 v[12:15], v[184:187], v[44:47], 0
	s_waitcnt lgkmcnt(3)
	v_mfma_f32_16x16x32_bf16 v[4:7], v[184:187], v[36:39], 0
	s_waitcnt lgkmcnt(2)
	v_mfma_f32_16x16x32_bf16 v[12:15], v[188:191], v[40:43], v[12:15]
	s_waitcnt lgkmcnt(2)
	v_mfma_f32_16x16x32_bf16 v[4:7], v[188:191], v[32:35], v[4:7]
	s_nop 6
	v_cvt_pk_bf16_f32 v12, v12, v13
	v_cvt_pk_bf16_f32 v13, v14, v15
	v_cvt_pk_bf16_f32 v4, v4, v5
	v_cvt_pk_bf16_f32 v5, v6, v7
	v_lshl_add_u64 v[6:7], v[84:85], 0, v[0:1]
	global_store_dwordx2 v[2:3], v[12:13], off offset:3072
	global_store_dwordx2 v[6:7], v[4:5], off
	s_waitcnt lgkmcnt(1)
	v_mfma_f32_16x16x32_bf16 v[12:15], v[192:195], v[44:47], 0
	v_lshl_add_u64 v[0:1], v[86:87], 0, v[0:1]
	s_waitcnt lgkmcnt(0)
	v_mfma_f32_16x16x32_bf16 v[12:15], v[196:199], v[40:43], v[12:15]
	s_nop 7
	v_cvt_pk_bf16_f32 v12, v12, v13
	v_cvt_pk_bf16_f32 v13, v14, v15
	global_store_dwordx2 v[2:3], v[12:13], off offset:3584
	s_waitcnt lgkmcnt(1)
	v_mfma_f32_16x16x32_bf16 v[2:5], v[192:195], v[36:39], 0
	s_waitcnt lgkmcnt(0)
	v_mfma_f32_16x16x32_bf16 v[2:5], v[196:199], v[32:35], v[2:5]
	s_nop 7
	v_cvt_pk_bf16_f32 v2, v2, v3
	v_cvt_pk_bf16_f32 v3, v4, v5
	global_store_dwordx2 v[0:1], v[2:3], off
	s_cbranch_scc0 .LBB0_836

.LBB0_910:
	s_or_b64 exec, exec, s[86:87]
	s_waitcnt lgkmcnt(0)
	s_barrier
	ds_read_b128 v[136:139], v103 offset:32768
	ds_read_b128 v[140:143], v104 offset:50176
	ds_read_b128 v[144:147], v104 offset:51264
	ds_read_b128 v[148:151], v103 offset:32832
	ds_read_b128 v[152:155], v104 offset:50240
	ds_read_b128 v[156:159], v104 offset:51328
	ds_read_b128 v[160:163], v103 offset:32896
	ds_read_b128 v[164:167], v104 offset:50304
	ds_read_b128 v[168:171], v104 offset:51392
	ds_read_b128 v[172:175], v103 offset:32960
	ds_read_b128 v[176:179], v104 offset:50368
	ds_read_b128 v[180:183], v104 offset:51456
	s_waitcnt lgkmcnt(10)
	v_mfma_f32_16x16x32_bf16 v[4:7], v[140:143], v[136:139], 0
	s_lshl_b32 s76, s91, 5
	s_waitcnt lgkmcnt(9)
	v_mfma_f32_16x16x32_bf16 v[0:3], v[144:147], v[136:139], 0
	s_waitcnt lgkmcnt(7)
	v_mfma_f32_16x16x32_bf16 v[4:7], v[152:155], v[148:151], v[4:7]
	s_waitcnt lgkmcnt(6)
	v_mfma_f32_16x16x32_bf16 v[0:3], v[156:159], v[148:151], v[0:3]
	s_waitcnt lgkmcnt(4)
	v_mfma_f32_16x16x32_bf16 v[4:7], v[164:167], v[160:163], v[4:7]
	s_waitcnt lgkmcnt(3)
	v_mfma_f32_16x16x32_bf16 v[0:3], v[168:171], v[160:163], v[0:3]
	s_waitcnt lgkmcnt(1)
	v_mfma_f32_16x16x32_bf16 v[4:7], v[176:179], v[172:175], v[4:7]
	v_add_u32_e32 v14, 0, v94
	s_waitcnt lgkmcnt(0)
	v_mfma_f32_16x16x32_bf16 v[0:3], v[180:183], v[172:175], v[0:3]
	v_cndmask_b32_e64 v8, 0, 1, s[8:9]
	v_cndmask_b32_e64 v9, 0, 1, s[10:11]
	v_cndmask_b32_e64 v8, v9, v8, s[42:43]
	v_and_b32_e32 v8, 1, v8
	v_cmp_eq_u32_e32 vcc, 1, v8
	v_cndmask_b32_e64 v8, 0, 1, s[12:13]
	v_cndmask_b32_e64 v9, 0, 1, s[14:15]
	v_cndmask_b32_e64 v8, v9, v8, s[42:43]
	v_and_b32_e32 v8, 1, v8
	v_cndmask_b32_e32 v4, 0, v4, vcc
	v_cmp_eq_u32_e32 vcc, 1, v8
	v_cndmask_b32_e64 v8, 0, 1, s[16:17]
	v_cndmask_b32_e64 v9, 0, 1, s[18:19]
	v_cndmask_b32_e64 v8, v9, v8, s[42:43]
	v_and_b32_e32 v8, 1, v8
	v_cndmask_b32_e32 v5, 0, v5, vcc
	v_cmp_eq_u32_e32 vcc, 1, v8
	v_cndmask_b32_e64 v8, 0, 1, s[20:21]
	v_cndmask_b32_e64 v9, 0, 1, s[22:23]
	v_cndmask_b32_e64 v8, v9, v8, s[42:43]
	v_and_b32_e32 v8, 1, v8
	v_cndmask_b32_e32 v6, 0, v6, vcc
	v_cmp_eq_u32_e32 vcc, 1, v8
	v_cndmask_b32_e64 v8, 0, 1, s[24:25]
	v_cndmask_b32_e64 v9, 0, 1, s[26:27]
	v_cndmask_b32_e64 v8, v9, v8, s[42:43]
	v_and_b32_e32 v8, 1, v8
	v_cndmask_b32_e32 v7, 0, v7, vcc
	v_cmp_eq_u32_e32 vcc, 1, v8
	v_cndmask_b32_e64 v9, 0, 1, s[30:31]
	s_nop 0
	v_cndmask_b32_e32 v8, 0, v0, vcc
	v_cndmask_b32_e64 v0, 0, 1, s[28:29]
	v_cndmask_b32_e64 v0, v9, v0, s[42:43]
	v_and_b32_e32 v0, 1, v0
	v_cmp_eq_u32_e32 vcc, 1, v0
	v_cndmask_b32_e64 v0, 0, 1, s[34:35]
	s_nop 0
	v_cndmask_b32_e32 v9, 0, v1, vcc
	v_cndmask_b32_e64 v1, 0, 1, s[36:37]
	v_cndmask_b32_e64 v0, v1, v0, s[42:43]
	v_and_b32_e32 v0, 1, v0
	v_cmp_eq_u32_e32 vcc, 1, v0
	v_cndmask_b32_e64 v0, 0, 1, s[38:39]
	v_cndmask_b32_e64 v1, 0, 1, s[40:41]
	v_cndmask_b32_e64 v0, v1, v0, s[42:43]
	v_and_b32_e32 v0, 1, v0
	v_cndmask_b32_e32 v10, 0, v2, vcc
	v_cmp_eq_u32_e32 vcc, 1, v0
	v_cvt_pk_bf16_f32 v0, v4, v5
	v_cvt_pk_bf16_f32 v1, v6, v7
	v_cndmask_b32_e32 v3, 0, v3, vcc
	v_cvt_pk_bf16_f32 v2, v8, v9
	v_cvt_pk_bf16_f32 v3, v10, v3
	v_add_u32_e32 v4, s90, v94
	ds_write_b128 v4, v[0:3]
	v_add_u32_e32 v0, 0x15000, v14
	s_waitcnt lgkmcnt(0)
	s_barrier
	ds_read_b128 v[0:3], v0
	s_lshl_b64 s[84:85], s[84:85], 11
	v_lshlrev_b32_e32 v8, 5, v56
	v_mov_b32_e32 v9, v97
	v_lshl_add_u64 v[8:9], s[84:85], 0, v[8:9]
	v_add_u32_e32 v4, 0x16000, v14
	v_lshl_add_u64 v[10:11], v[70:71], 0, s[76:77]
	ds_read_b128 v[4:7], v4
	v_lshl_add_u64 v[12:13], v[10:11], 0, v[8:9]
	s_waitcnt lgkmcnt(1)
	v_mfma_f32_16x16x32_bf16 v[8:11], v[44:47], v[0:3], 0
	s_lshl_b64 s[42:43], s[78:79], 16
	s_add_i32 s78, s78, s96
	s_cmpk_lt_i32 s78, 0x480
	v_mfma_f32_16x16x32_bf16 v[0:3], v[36:39], v[0:3], 0
	s_waitcnt lgkmcnt(0)
	v_mfma_f32_16x16x32_bf16 v[0:3], v[32:35], v[4:7], v[0:3]
	v_mfma_f32_16x16x32_bf16 v[8:11], v[40:43], v[4:7], v[8:11]
	v_add_u32_e32 v4, 0x16400, v14
	s_nop 5
	v_cvt_pk_bf16_f32 v0, v0, v1
	v_cvt_pk_bf16_f32 v1, v2, v3
	global_store_dwordx2 v[12:13], v[0:1], off offset:512
	v_add_u32_e32 v0, 0x15400, v14
	ds_read_b128 v[0:3], v0
	ds_read_b128 v[4:7], v4
	v_cvt_pk_bf16_f32 v8, v8, v9
	v_cvt_pk_bf16_f32 v9, v10, v11
	global_store_dwordx2 v[12:13], v[8:9], off
	s_waitcnt lgkmcnt(1)
	v_mfma_f32_16x16x32_bf16 v[8:11], v[44:47], v[0:3], 0
	v_mfma_f32_16x16x32_bf16 v[0:3], v[36:39], v[0:3], 0
	s_waitcnt lgkmcnt(0)
	v_mfma_f32_16x16x32_bf16 v[8:11], v[40:43], v[4:7], v[8:11]
	v_mfma_f32_16x16x32_bf16 v[0:3], v[32:35], v[4:7], v[0:3]
	v_add_u32_e32 v4, 0x16800, v14
	s_nop 5
	v_cvt_pk_bf16_f32 v8, v8, v9
	v_cvt_pk_bf16_f32 v9, v10, v11
	v_add_co_u32_e32 v10, vcc, s65, v12
	ds_read_b128 v[4:7], v4
	s_nop 0
	v_addc_co_u32_e32 v11, vcc, 0, v13, vcc
	v_cvt_pk_bf16_f32 v0, v0, v1
	v_cvt_pk_bf16_f32 v1, v2, v3
	global_store_dwordx2 v[10:11], v[0:1], off offset:512
	v_add_u32_e32 v0, 0x15800, v14
	ds_read_b128 v[0:3], v0
	global_store_dwordx2 v[10:11], v[8:9], off
	s_waitcnt lgkmcnt(0)
	v_mfma_f32_16x16x32_bf16 v[8:11], v[44:47], v[0:3], 0
	v_mfma_f32_16x16x32_bf16 v[0:3], v[36:39], v[0:3], 0
	v_mfma_f32_16x16x32_bf16 v[8:11], v[40:43], v[4:7], v[8:11]
	v_mfma_f32_16x16x32_bf16 v[0:3], v[32:35], v[4:7], v[0:3]
	v_add_u32_e32 v4, 0x16c00, v14
	s_nop 5
	v_cvt_pk_bf16_f32 v8, v8, v9
	v_cvt_pk_bf16_f32 v9, v10, v11
	v_add_co_u32_e32 v10, vcc, s49, v12
	ds_read_b128 v[4:7], v4
	s_nop 0
	v_addc_co_u32_e32 v11, vcc, 0, v13, vcc
	v_cvt_pk_bf16_f32 v0, v0, v1
	v_cvt_pk_bf16_f32 v1, v2, v3
	global_store_dwordx2 v[10:11], v[0:1], off offset:512
	v_add_u32_e32 v0, 0x15c00, v14
	ds_read_b128 v[0:3], v0
	global_store_dwordx2 v[10:11], v[8:9], off
	s_waitcnt lgkmcnt(0)
	v_mfma_f32_16x16x32_bf16 v[8:11], v[44:47], v[0:3], 0
	v_mfma_f32_16x16x32_bf16 v[0:3], v[36:39], v[0:3], 0
	v_mfma_f32_16x16x32_bf16 v[8:11], v[40:43], v[4:7], v[8:11]
	v_mfma_f32_16x16x32_bf16 v[0:3], v[32:35], v[4:7], v[0:3]
	s_nop 6
	v_cvt_pk_bf16_f32 v8, v8, v9
	v_cvt_pk_bf16_f32 v9, v10, v11
	v_add_co_u32_e32 v10, vcc, s64, v12
	v_cvt_pk_bf16_f32 v0, v0, v1
	s_nop 0
	v_addc_co_u32_e32 v11, vcc, 0, v13, vcc
	v_cvt_pk_bf16_f32 v1, v2, v3
	global_store_dwordx2 v[10:11], v[8:9], off
	global_store_dwordx2 v[10:11], v[0:1], off offset:512
	ds_read_b128 v[136:139], v105
	ds_read_b128 v[140:143], v105 offset:64
	ds_read_b128 v[144:147], v105 offset:2304
	ds_read_b128 v[148:151], v105 offset:2368
	ds_read_b128 v[152:155], v105 offset:4608
	ds_read_b128 v[156:159], v105 offset:4672
	ds_read_b128 v[160:163], v105 offset:6912
	ds_read_b128 v[164:167], v105 offset:6976
	ds_read_b128 v[168:171], v105 offset:9216
	ds_read_b128 v[172:175], v105 offset:9280
	ds_read_b128 v[176:179], v105 offset:11520
	ds_read_b128 v[180:183], v105 offset:11584
	ds_read_b128 v[184:187], v105 offset:13824
	ds_read_b128 v[188:191], v105 offset:13888
	ds_read_b128 v[192:195], v105 offset:16128
	ds_read_b128 v[196:199], v105 offset:16192
	s_waitcnt lgkmcnt(15)
	v_mfma_f32_16x16x32_bf16 v[0:3], v[136:139], v[44:47], 0
	s_waitcnt lgkmcnt(15)
	v_mfma_f32_16x16x32_bf16 v[4:7], v[136:139], v[36:39], 0
	s_waitcnt lgkmcnt(14)
	v_mfma_f32_16x16x32_bf16 v[0:3], v[140:143], v[40:43], v[0:3]
	s_waitcnt lgkmcnt(14)
	v_mfma_f32_16x16x32_bf16 v[4:7], v[140:143], v[32:35], v[4:7]
	s_nop 6
	v_cvt_pk_bf16_f32 v12, v0, v1
	v_lshl_add_u64 v[0:1], s[42:43], 0, v[88:89]
	v_cvt_pk_bf16_f32 v13, v2, v3
	v_lshl_add_u64 v[2:3], v[72:73], 0, v[0:1]
	v_or_b32_e32 v0, 0x1000, v0
	v_cvt_pk_bf16_f32 v4, v4, v5
	v_cvt_pk_bf16_f32 v5, v6, v7
	v_lshl_add_u64 v[6:7], v[72:73], 0, v[0:1]
	global_store_dwordx2 v[2:3], v[12:13], off
	global_store_dwordx2 v[6:7], v[4:5], off
	s_waitcnt lgkmcnt(13)
	v_mfma_f32_16x16x32_bf16 v[12:15], v[144:147], v[44:47], 0
	s_waitcnt lgkmcnt(13)
	v_mfma_f32_16x16x32_bf16 v[4:7], v[144:147], v[36:39], 0
	s_waitcnt lgkmcnt(12)
	v_mfma_f32_16x16x32_bf16 v[12:15], v[148:151], v[40:43], v[12:15]
	s_waitcnt lgkmcnt(12)
	v_mfma_f32_16x16x32_bf16 v[4:7], v[148:151], v[32:35], v[4:7]
	s_nop 6
	v_cvt_pk_bf16_f32 v12, v12, v13
	v_cvt_pk_bf16_f32 v13, v14, v15
	v_cvt_pk_bf16_f32 v4, v4, v5
	v_cvt_pk_bf16_f32 v5, v6, v7
	v_lshl_add_u64 v[6:7], v[74:75], 0, v[0:1]
	global_store_dwordx2 v[2:3], v[12:13], off offset:512
	global_store_dwordx2 v[6:7], v[4:5], off
	s_waitcnt lgkmcnt(11)
	v_mfma_f32_16x16x32_bf16 v[12:15], v[152:155], v[44:47], 0
	s_waitcnt lgkmcnt(11)
	v_mfma_f32_16x16x32_bf16 v[4:7], v[152:155], v[36:39], 0
	s_waitcnt lgkmcnt(10)
	v_mfma_f32_16x16x32_bf16 v[12:15], v[156:159], v[40:43], v[12:15]
	s_waitcnt lgkmcnt(10)
	v_mfma_f32_16x16x32_bf16 v[4:7], v[156:159], v[32:35], v[4:7]
	s_nop 6
	v_cvt_pk_bf16_f32 v12, v12, v13
	v_cvt_pk_bf16_f32 v13, v14, v15
	v_cvt_pk_bf16_f32 v4, v4, v5
	v_cvt_pk_bf16_f32 v5, v6, v7
	v_lshl_add_u64 v[6:7], v[76:77], 0, v[0:1]
	global_store_dwordx2 v[2:3], v[12:13], off offset:1024
	global_store_dwordx2 v[6:7], v[4:5], off
	s_waitcnt lgkmcnt(9)
	v_mfma_f32_16x16x32_bf16 v[12:15], v[160:163], v[44:47], 0
	s_waitcnt lgkmcnt(9)
	v_mfma_f32_16x16x32_bf16 v[4:7], v[160:163], v[36:39], 0
	s_waitcnt lgkmcnt(8)
	v_mfma_f32_16x16x32_bf16 v[12:15], v[164:167], v[40:43], v[12:15]
	s_waitcnt lgkmcnt(8)
	v_mfma_f32_16x16x32_bf16 v[4:7], v[164:167], v[32:35], v[4:7]
	s_nop 6
	v_cvt_pk_bf16_f32 v12, v12, v13
	v_cvt_pk_bf16_f32 v13, v14, v15
	v_cvt_pk_bf16_f32 v4, v4, v5
	v_cvt_pk_bf16_f32 v5, v6, v7
	v_lshl_add_u64 v[6:7], v[78:79], 0, v[0:1]
	global_store_dwordx2 v[2:3], v[12:13], off offset:1536
	global_store_dwordx2 v[6:7], v[4:5], off
	s_waitcnt lgkmcnt(7)
	v_mfma_f32_16x16x32_bf16 v[12:15], v[168:171], v[44:47], 0
	s_waitcnt lgkmcnt(7)
	v_mfma_f32_16x16x32_bf16 v[4:7], v[168:171], v[36:39], 0
	s_waitcnt lgkmcnt(6)
	v_mfma_f32_16x16x32_bf16 v[12:15], v[172:175], v[40:43], v[12:15]
	s_waitcnt lgkmcnt(6)
	v_mfma_f32_16x16x32_bf16 v[4:7], v[172:175], v[32:35], v[4:7]
	s_nop 6
	v_cvt_pk_bf16_f32 v12, v12, v13
	v_cvt_pk_bf16_f32 v13, v14, v15
	v_cvt_pk_bf16_f32 v4, v4, v5
	v_cvt_pk_bf16_f32 v5, v6, v7
	v_lshl_add_u64 v[6:7], v[80:81], 0, v[0:1]
	global_store_dwordx2 v[2:3], v[12:13], off offset:2048
	global_store_dwordx2 v[6:7], v[4:5], off
	s_waitcnt lgkmcnt(5)
	v_mfma_f32_16x16x32_bf16 v[12:15], v[176:179], v[44:47], 0
	s_waitcnt lgkmcnt(5)
	v_mfma_f32_16x16x32_bf16 v[4:7], v[176:179], v[36:39], 0
	s_waitcnt lgkmcnt(4)
	v_mfma_f32_16x16x32_bf16 v[12:15], v[180:183], v[40:43], v[12:15]
	s_waitcnt lgkmcnt(4)
	v_mfma_f32_16x16x32_bf16 v[4:7], v[180:183], v[32:35], v[4:7]
	s_nop 6
	v_cvt_pk_bf16_f32 v12, v12, v13
	v_cvt_pk_bf16_f32 v13, v14, v15
	v_cvt_pk_bf16_f32 v4, v4, v5
	v_cvt_pk_bf16_f32 v5, v6, v7
	v_lshl_add_u64 v[6:7], v[82:83], 0, v[0:1]
	global_store_dwordx2 v[2:3], v[12:13], off offset:2560
	global_store_dwordx2 v[6:7], v[4:5], off
	s_waitcnt lgkmcnt(3)
	v_mfma_f32_16x16x32_bf16 v[12:15], v[184:187], v[44:47], 0
	s_waitcnt lgkmcnt(3)
	v_mfma_f32_16x16x32_bf16 v[4:7], v[184:187], v[36:39], 0
	s_waitcnt lgkmcnt(2)
	v_mfma_f32_16x16x32_bf16 v[12:15], v[188:191], v[40:43], v[12:15]
	s_waitcnt lgkmcnt(2)
	v_mfma_f32_16x16x32_bf16 v[4:7], v[188:191], v[32:35], v[4:7]
	s_nop 6
	v_cvt_pk_bf16_f32 v12, v12, v13
	v_cvt_pk_bf16_f32 v13, v14, v15
	v_cvt_pk_bf16_f32 v4, v4, v5
	v_cvt_pk_bf16_f32 v5, v6, v7
	v_lshl_add_u64 v[6:7], v[84:85], 0, v[0:1]
	global_store_dwordx2 v[2:3], v[12:13], off offset:3072
	global_store_dwordx2 v[6:7], v[4:5], off
	s_waitcnt lgkmcnt(1)
	v_mfma_f32_16x16x32_bf16 v[12:15], v[192:195], v[44:47], 0
	v_lshl_add_u64 v[0:1], v[86:87], 0, v[0:1]
	s_waitcnt lgkmcnt(0)
	v_mfma_f32_16x16x32_bf16 v[12:15], v[196:199], v[40:43], v[12:15]
	s_nop 7
	v_cvt_pk_bf16_f32 v12, v12, v13
	v_cvt_pk_bf16_f32 v13, v14, v15
	global_store_dwordx2 v[2:3], v[12:13], off offset:3584
	s_waitcnt lgkmcnt(1)
	v_mfma_f32_16x16x32_bf16 v[2:5], v[192:195], v[36:39], 0
	s_waitcnt lgkmcnt(0)
	v_mfma_f32_16x16x32_bf16 v[2:5], v[196:199], v[32:35], v[2:5]
	s_nop 7
	v_cvt_pk_bf16_f32 v2, v2, v3
	v_cvt_pk_bf16_f32 v3, v4, v5
	global_store_dwordx2 v[0:1], v[2:3], off
	s_cbranch_scc0 .LBB0_933
